# v15 + first-trip SrcC=0 peel also in the two gather (gate/up) GEMM K-loops
# speedup vs baseline: 1.0222x; 1.0056x over previous
.LBB0_1943:
	s_add_u32 s8, s36, 0x100
	v_mov_b32_e32 v48, 0
	s_addc_u32 s23, s37, 0
	s_mov_b32 s60, -2
	s_mov_b64 s[36:37], s[16:17]
	s_branch .Lpeelg_h0

.LBB0_1945:
	ds_read_b128 v[0:3], v193
	ds_read_b128 v[4:7], v193 offset:1024
	ds_read_b128 v[8:11], v193 offset:2048
	ds_read_b128 v[12:15], v193 offset:3072
	s_cmp_eq_u32 s60, 12
	s_cselect_b64 s[38:39], -1, 0
	v_mov_b32_e32 v178, v186
	ds_read_b128 v[40:43], v194
	ds_read_b128 v[44:47], v194 offset:1024
	ds_read_b128 v[32:35], v194 offset:2048
	ds_read_b128 v[36:39], v194 offset:3072
	ds_read_b128 v[24:27], v194 offset:4096
	ds_read_b128 v[28:31], v194 offset:5120
	ds_read_b128 v[16:19], v194 offset:6144
	ds_read_b128 v[20:23], v194 offset:7168
	s_add_i32 m0, s31, 0xc000
	s_nop 0
	global_load_lds_dwordx4 v178, s[36:37]
	v_mov_b32_e32 v178, v187
	s_add_i32 m0, s31, 0xe000
	s_nop 0
	global_load_lds_dwordx4 v178, s[36:37]
	s_waitcnt lgkmcnt(8)
	s_barrier
	s_waitcnt lgkmcnt(0)
	s_setprio 1
	s_setprio 0
	s_barrier
	s_and_b64 s[40:41], s[34:35], s[38:39]
	s_andn2_b64 vcc, exec, s[40:41]
	s_cbranch_vccnz .LBB0_1944
	ds_read_b32 v178, v189
	ds_read_b32 v185, v190
	ds_read_b32 v186, v191
	ds_read_b32 v187, v192
	s_waitcnt lgkmcnt(0)
	v_lshl_add_u32 v184, v178, 11, v180
	v_lshl_add_u32 v185, v185, 11, v182
	v_lshl_add_u32 v186, v186, 11, v180
	v_lshl_add_u32 v187, v187, 11, v182
	s_branch .LBB0_1944
.Lpeelg_h0:
	ds_read_b128 v[0:3], v193
	ds_read_b128 v[4:7], v193 offset:1024
	ds_read_b128 v[8:11], v193 offset:2048
	ds_read_b128 v[12:15], v193 offset:3072
	s_cmp_eq_u32 s60, 12
	s_cselect_b64 s[38:39], -1, 0
	v_mov_b32_e32 v178, v186
	ds_read_b128 v[40:43], v194
	ds_read_b128 v[44:47], v194 offset:1024
	ds_read_b128 v[32:35], v194 offset:2048
	ds_read_b128 v[36:39], v194 offset:3072
	ds_read_b128 v[24:27], v194 offset:4096
	ds_read_b128 v[28:31], v194 offset:5120
	ds_read_b128 v[16:19], v194 offset:6144
	ds_read_b128 v[20:23], v194 offset:7168
	s_add_i32 m0, s31, 0xc000
	s_nop 0
	global_load_lds_dwordx4 v178, s[36:37]
	v_mov_b32_e32 v178, v187
	s_add_i32 m0, s31, 0xe000
	s_nop 0
	global_load_lds_dwordx4 v178, s[36:37]
	s_waitcnt lgkmcnt(8)
	s_barrier
	s_waitcnt lgkmcnt(0)
	s_setprio 1
	s_setprio 0
	s_barrier
	s_and_b64 s[40:41], s[34:35], s[38:39]
	s_andn2_b64 vcc, exec, s[40:41]
	s_cbranch_vccnz .Lpeelg_t0
	ds_read_b32 v178, v189
	ds_read_b32 v185, v190
	ds_read_b32 v186, v191
	ds_read_b32 v187, v192
	s_waitcnt lgkmcnt(0)
	v_lshl_add_u32 v184, v178, 11, v180
	v_lshl_add_u32 v185, v185, 11, v182
	v_lshl_add_u32 v186, v186, 11, v180
	v_lshl_add_u32 v187, v187, 11, v182
	s_branch .Lpeelg_t0
.Lpeelg_t0:
	s_add_u32 s40, s36, 0x80
	s_addc_u32 s41, s37, 0
	v_add_u32_e32 v178, s5, v188
	s_and_b64 s[38:39], s[38:39], exec
	ds_read_b128 v[196:199], v178
	ds_read_b128 v[200:203], v178 offset:1024
	ds_read_b128 v[204:207], v178 offset:2048
	ds_read_b128 v[208:211], v178 offset:3072
	v_mov_b32_e32 v178, v181
	s_mov_b32 m0, s43
	s_cselect_b32 s39, s27, s23
	s_cselect_b32 s38, s26, s8
	s_waitcnt lgkmcnt(0)
	v_mfma_scale_f32_16x16x128_f8f6f4 v[172:175], v[0:7], v[40:47], 0, v195, v195 op_sel_hi:[0,0,0]
	global_load_lds_dwordx4 v178, s[38:39]
	v_mov_b32_e32 v178, v183
	s_mov_b32 m0, s44
	s_cselect_b32 s41, s11, s41
	global_load_lds_dwordx4 v178, s[38:39]
	v_mfma_scale_f32_16x16x128_f8f6f4 v[168:171], v[8:15], v[40:47], 0, v195, v195 op_sel_hi:[0,0,0]
	s_barrier
	s_waitcnt lgkmcnt(0)
	s_cselect_b32 s40, s10, s40
	v_mfma_scale_f32_16x16x128_f8f6f4 v[164:167], v[0:7], v[32:39], 0, v195, v195 op_sel_hi:[0,0,0]
	v_mfma_scale_f32_16x16x128_f8f6f4 v[156:159], v[8:15], v[32:39], 0, v195, v195 op_sel_hi:[0,0,0]
	v_mfma_scale_f32_16x16x128_f8f6f4 v[140:143], v[0:7], v[24:31], 0, v195, v195 op_sel_hi:[0,0,0]
	v_mfma_scale_f32_16x16x128_f8f6f4 v[132:135], v[8:15], v[24:31], 0, v195, v195 op_sel_hi:[0,0,0]
	v_mfma_scale_f32_16x16x128_f8f6f4 v[120:123], v[0:7], v[16:23], 0, v195, v195 op_sel_hi:[0,0,0]
	v_mfma_scale_f32_16x16x128_f8f6f4 v[112:115], v[8:15], v[16:23], 0, v195, v195 op_sel_hi:[0,0,0]
	s_setprio 1
	v_mfma_scale_f32_16x16x128_f8f6f4 v[160:163], v[196:203], v[40:47], 0, v195, v195 op_sel_hi:[0,0,0]
	v_mfma_scale_f32_16x16x128_f8f6f4 v[152:155], v[204:211], v[40:47], 0, v195, v195 op_sel_hi:[0,0,0]
	v_mfma_scale_f32_16x16x128_f8f6f4 v[148:151], v[196:203], v[32:39], 0, v195, v195 op_sel_hi:[0,0,0]
	v_mfma_scale_f32_16x16x128_f8f6f4 v[144:147], v[204:211], v[32:39], 0, v195, v195 op_sel_hi:[0,0,0]
	v_mfma_scale_f32_16x16x128_f8f6f4 v[136:139], v[196:203], v[24:31], 0, v195, v195 op_sel_hi:[0,0,0]
	v_mfma_scale_f32_16x16x128_f8f6f4 v[128:131], v[204:211], v[24:31], 0, v195, v195 op_sel_hi:[0,0,0]
	v_mfma_scale_f32_16x16x128_f8f6f4 v[124:127], v[196:203], v[16:23], 0, v195, v195 op_sel_hi:[0,0,0]
	v_mfma_scale_f32_16x16x128_f8f6f4 v[116:119], v[204:211], v[16:23], 0, v195, v195 op_sel_hi:[0,0,0]
	s_setprio 0
	v_mov_b32_e32 v178, v184
	s_mov_b32 m0, s31
	s_barrier
	ds_read_b128 v[16:19], v194 offset:16384
	ds_read_b128 v[20:23], v194 offset:17408
	ds_read_b128 v[24:27], v194 offset:18432
	ds_read_b128 v[28:31], v194 offset:19456
	ds_read_b128 v[32:35], v194 offset:20480
	ds_read_b128 v[36:39], v194 offset:21504
	ds_read_b128 v[40:43], v194 offset:22528
	ds_read_b128 v[44:47], v194 offset:23552
	s_nop 0
	global_load_lds_dwordx4 v178, s[40:41]
	v_mov_b32_e32 v178, v185
	s_mov_b32 m0, s45
	s_nop 0
	global_load_lds_dwordx4 v178, s[40:41]
	s_barrier
	s_waitcnt lgkmcnt(0)
	s_setprio 1
	s_waitcnt lgkmcnt(0)
	v_mfma_scale_f32_16x16x128_f8f6f4 v[108:111], v[0:7], v[16:23], 0, v195, v195 op_sel_hi:[0,0,0]
	v_mfma_scale_f32_16x16x128_f8f6f4 v[100:103], v[8:15], v[16:23], 0, v195, v195 op_sel_hi:[0,0,0]
	v_mfma_scale_f32_16x16x128_f8f6f4 v[92:95], v[0:7], v[24:31], 0, v195, v195 op_sel_hi:[0,0,0]
	v_mfma_scale_f32_16x16x128_f8f6f4 v[84:87], v[8:15], v[24:31], 0, v195, v195 op_sel_hi:[0,0,0]
	v_mfma_scale_f32_16x16x128_f8f6f4 v[76:79], v[0:7], v[32:39], 0, v195, v195 op_sel_hi:[0,0,0]
	v_mfma_scale_f32_16x16x128_f8f6f4 v[68:71], v[8:15], v[32:39], 0, v195, v195 op_sel_hi:[0,0,0]
	v_mfma_scale_f32_16x16x128_f8f6f4 v[60:63], v[0:7], v[40:47], 0, v195, v195 op_sel_hi:[0,0,0]
	v_mfma_scale_f32_16x16x128_f8f6f4 v[52:55], v[8:15], v[40:47], 0, v195, v195 op_sel_hi:[0,0,0]
	s_setprio 0
	s_barrier
	s_add_u32 s62, s38, 0x40000
	s_addc_u32 s63, s39, 0
	v_mov_b32_e32 v0, v181
	s_add_i32 s61, s5, s42
	s_mov_b32 m0, s61
	s_nop 0
	global_load_lds_dwordx4 v0, s[62:63]
	v_mov_b32_e32 v0, v183
	s_add_i32 m0, s61, 0x2000
	s_nop 0
	global_load_lds_dwordx4 v0, s[62:63]
	s_waitcnt vmcnt(6)
	s_barrier
	s_setprio 1
	v_mfma_scale_f32_16x16x128_f8f6f4 v[104:107], v[196:203], v[16:23], 0, v195, v195 op_sel_hi:[0,0,0]
	v_mfma_scale_f32_16x16x128_f8f6f4 v[96:99], v[204:211], v[16:23], 0, v195, v195 op_sel_hi:[0,0,0]
	v_mfma_scale_f32_16x16x128_f8f6f4 v[88:91], v[196:203], v[24:31], 0, v195, v195 op_sel_hi:[0,0,0]
	v_mfma_scale_f32_16x16x128_f8f6f4 v[80:83], v[204:211], v[24:31], 0, v195, v195 op_sel_hi:[0,0,0]
	v_mfma_scale_f32_16x16x128_f8f6f4 v[72:75], v[196:203], v[32:39], 0, v195, v195 op_sel_hi:[0,0,0]
	v_mfma_scale_f32_16x16x128_f8f6f4 v[64:67], v[204:211], v[32:39], 0, v195, v195 op_sel_hi:[0,0,0]
	v_mfma_scale_f32_16x16x128_f8f6f4 v[56:59], v[196:203], v[40:47], 0, v195, v195 op_sel_hi:[0,0,0]
	v_mfma_scale_f32_16x16x128_f8f6f4 v[48:51], v[204:211], v[40:47], 0, v195, v195 op_sel_hi:[0,0,0]
	s_setprio 0
	s_add_i32 s61, 0, 0x18000
	v_add_u32_e32 v12, s61, v188
	s_barrier
	ds_read_b128 v[0:3], v12
	ds_read_b128 v[4:7], v12 offset:1024
	ds_read_b128 v[8:11], v12 offset:2048
	ds_read_b128 v[12:15], v12 offset:3072
	v_mov_b32_e32 v178, v186
	s_mov_b32 m0, s46
	ds_read_b128 v[16:19], v194 offset:32768
	ds_read_b128 v[20:23], v194 offset:33792
	ds_read_b128 v[24:27], v194 offset:34816
	ds_read_b128 v[28:31], v194 offset:35840
	ds_read_b128 v[32:35], v194 offset:36864
	ds_read_b128 v[36:39], v194 offset:37888
	ds_read_b128 v[40:43], v194 offset:38912
	ds_read_b128 v[44:47], v194 offset:39936
	s_nop 0
	global_load_lds_dwordx4 v178, s[40:41]
	v_mov_b32_e32 v178, v187
	s_mov_b32 m0, s47
	s_nop 0
	global_load_lds_dwordx4 v178, s[40:41]
	s_waitcnt lgkmcnt(8)
	s_barrier
	s_waitcnt lgkmcnt(0)
	s_setprio 1
	s_waitcnt lgkmcnt(0)
	v_mfma_scale_f32_16x16x128_f8f6f4 v[172:175], v[0:7], v[16:23], v[172:175], v195, v195 op_sel_hi:[0,0,0]
	v_mfma_scale_f32_16x16x128_f8f6f4 v[168:171], v[8:15], v[16:23], v[168:171], v195, v195 op_sel_hi:[0,0,0]
	v_mfma_scale_f32_16x16x128_f8f6f4 v[164:167], v[0:7], v[24:31], v[164:167], v195, v195 op_sel_hi:[0,0,0]
	v_mfma_scale_f32_16x16x128_f8f6f4 v[156:159], v[8:15], v[24:31], v[156:159], v195, v195 op_sel_hi:[0,0,0]
	v_mfma_scale_f32_16x16x128_f8f6f4 v[140:143], v[0:7], v[32:39], v[140:143], v195, v195 op_sel_hi:[0,0,0]
	v_mfma_scale_f32_16x16x128_f8f6f4 v[132:135], v[8:15], v[32:39], v[132:135], v195, v195 op_sel_hi:[0,0,0]
	v_mfma_scale_f32_16x16x128_f8f6f4 v[120:123], v[0:7], v[40:47], v[120:123], v195, v195 op_sel_hi:[0,0,0]
	v_mfma_scale_f32_16x16x128_f8f6f4 v[112:115], v[8:15], v[40:47], v[112:115], v195, v195 op_sel_hi:[0,0,0]
	s_setprio 0
	s_barrier
	s_add_i32 s62, 0, 0x1c000
	v_add_u32_e32 v178, s62, v188
	ds_read_b128 v[196:199], v178
	ds_read_b128 v[200:203], v178 offset:1024
	ds_read_b128 v[204:207], v178 offset:2048
	ds_read_b128 v[208:211], v178 offset:3072
	v_mov_b32_e32 v178, v181
	s_add_i32 s61, s61, s42
	v_lshl_add_u64 v[212:213], s[38:39], 0, v[178:179]
	v_lshl_add_u64 v[212:213], v[212:213], 0, s[12:13]
	s_mov_b32 m0, s61
	v_mov_b32_e32 v178, v183
	global_load_lds_dwordx4 v[212:213], off
	s_add_i32 m0, s61, 0x2000
	v_lshl_add_u64 v[212:213], s[38:39], 0, v[178:179]
	v_lshl_add_u64 v[212:213], v[212:213], 0, s[12:13]
	global_load_lds_dwordx4 v[212:213], off
	s_barrier
	s_waitcnt lgkmcnt(0)
	s_setprio 1
	s_waitcnt lgkmcnt(0)
	v_mfma_scale_f32_16x16x128_f8f6f4 v[160:163], v[196:203], v[16:23], v[160:163], v195, v195 op_sel_hi:[0,0,0]
	v_mfma_scale_f32_16x16x128_f8f6f4 v[152:155], v[204:211], v[16:23], v[152:155], v195, v195 op_sel_hi:[0,0,0]
	v_mfma_scale_f32_16x16x128_f8f6f4 v[148:151], v[196:203], v[24:31], v[148:151], v195, v195 op_sel_hi:[0,0,0]
	v_mfma_scale_f32_16x16x128_f8f6f4 v[144:147], v[204:211], v[24:31], v[144:147], v195, v195 op_sel_hi:[0,0,0]
	v_mfma_scale_f32_16x16x128_f8f6f4 v[136:139], v[196:203], v[32:39], v[136:139], v195, v195 op_sel_hi:[0,0,0]
	v_mfma_scale_f32_16x16x128_f8f6f4 v[128:131], v[204:211], v[32:39], v[128:131], v195, v195 op_sel_hi:[0,0,0]
	v_mfma_scale_f32_16x16x128_f8f6f4 v[124:127], v[196:203], v[40:47], v[124:127], v195, v195 op_sel_hi:[0,0,0]
	v_mfma_scale_f32_16x16x128_f8f6f4 v[116:119], v[204:211], v[40:47], v[116:119], v195, v195 op_sel_hi:[0,0,0]
	s_setprio 0
	v_mov_b32_e32 v178, v184
	s_barrier
	ds_read_b128 v[16:19], v194 offset:49152
	ds_read_b128 v[20:23], v194 offset:50176
	ds_read_b128 v[24:27], v194 offset:51200
	ds_read_b128 v[28:31], v194 offset:52224
	ds_read_b128 v[32:35], v194 offset:53248
	ds_read_b128 v[36:39], v194 offset:54272
	ds_read_b128 v[40:43], v194 offset:55296
	ds_read_b128 v[44:47], v194 offset:56320
	s_mov_b32 m0, s52
	v_lshl_add_u64 v[212:213], s[40:41], 0, v[178:179]
	v_lshl_add_u64 v[212:213], v[212:213], 0, s[12:13]
	v_mov_b32_e32 v178, v185
	global_load_lds_dwordx4 v[212:213], off
	s_mov_b32 m0, s53
	v_lshl_add_u64 v[212:213], s[40:41], 0, v[178:179]
	v_lshl_add_u64 v[212:213], v[212:213], 0, s[12:13]
	global_load_lds_dwordx4 v[212:213], off
	s_barrier
	s_waitcnt lgkmcnt(0)
	s_setprio 1
	s_waitcnt lgkmcnt(0)
	v_mfma_scale_f32_16x16x128_f8f6f4 v[108:111], v[0:7], v[16:23], v[108:111], v195, v195 op_sel_hi:[0,0,0]
	v_mfma_scale_f32_16x16x128_f8f6f4 v[100:103], v[8:15], v[16:23], v[100:103], v195, v195 op_sel_hi:[0,0,0]
	v_mfma_scale_f32_16x16x128_f8f6f4 v[92:95], v[0:7], v[24:31], v[92:95], v195, v195 op_sel_hi:[0,0,0]
	v_mfma_scale_f32_16x16x128_f8f6f4 v[84:87], v[8:15], v[24:31], v[84:87], v195, v195 op_sel_hi:[0,0,0]
	v_mfma_scale_f32_16x16x128_f8f6f4 v[76:79], v[0:7], v[32:39], v[76:79], v195, v195 op_sel_hi:[0,0,0]
	v_mfma_scale_f32_16x16x128_f8f6f4 v[68:71], v[8:15], v[32:39], v[68:71], v195, v195 op_sel_hi:[0,0,0]
	v_mfma_scale_f32_16x16x128_f8f6f4 v[60:63], v[0:7], v[40:47], v[60:63], v195, v195 op_sel_hi:[0,0,0]
	v_mfma_scale_f32_16x16x128_f8f6f4 v[52:55], v[8:15], v[40:47], v[52:55], v195, v195 op_sel_hi:[0,0,0]
	s_setprio 0
	s_barrier
	s_add_u32 s38, s38, 0x40080
	s_addc_u32 s39, s39, 0
	v_mov_b32_e32 v0, v181
	s_add_i32 s40, s62, s42
	s_mov_b32 m0, s40
	s_nop 0
	global_load_lds_dwordx4 v0, s[38:39]
	v_mov_b32_e32 v0, v183
	s_add_i32 m0, s40, 0x2000
	s_nop 0
	global_load_lds_dwordx4 v0, s[38:39]
	s_waitcnt vmcnt(6)
	s_barrier
	s_setprio 1
	v_mfma_scale_f32_16x16x128_f8f6f4 v[104:107], v[196:203], v[16:23], v[104:107], v195, v195 op_sel_hi:[0,0,0]
	v_mfma_scale_f32_16x16x128_f8f6f4 v[96:99], v[204:211], v[16:23], v[96:99], v195, v195 op_sel_hi:[0,0,0]
	v_mfma_scale_f32_16x16x128_f8f6f4 v[88:91], v[196:203], v[24:31], v[88:91], v195, v195 op_sel_hi:[0,0,0]
	v_mfma_scale_f32_16x16x128_f8f6f4 v[80:83], v[204:211], v[24:31], v[80:83], v195, v195 op_sel_hi:[0,0,0]
	v_mfma_scale_f32_16x16x128_f8f6f4 v[72:75], v[196:203], v[32:39], v[72:75], v195, v195 op_sel_hi:[0,0,0]
	v_mfma_scale_f32_16x16x128_f8f6f4 v[64:67], v[204:211], v[32:39], v[64:67], v195, v195 op_sel_hi:[0,0,0]
	v_mfma_scale_f32_16x16x128_f8f6f4 v[56:59], v[196:203], v[40:47], v[56:59], v195, v195 op_sel_hi:[0,0,0]
	v_mfma_scale_f32_16x16x128_f8f6f4 v[48:51], v[204:211], v[40:47], v[48:51], v195, v195 op_sel_hi:[0,0,0]
	s_setprio 0
	s_add_i32 s60, s60, 2
	s_add_u32 s36, s36, 0x100
	s_addc_u32 s37, s37, 0
	s_add_u32 s8, s8, 0x100
	s_addc_u32 s23, s23, 0
	s_cmp_gt_u32 s60, 13
	s_barrier
	s_cbranch_scc1 .LBB0_1936
	s_branch .LBB0_1945

.LBB0_5374:
	ds_read_b128 v[0:3], v193
	ds_read_b128 v[4:7], v193 offset:1024
	ds_read_b128 v[8:11], v193 offset:2048
	ds_read_b128 v[12:15], v193 offset:3072
	s_cmp_eq_u32 s60, 12
	s_cselect_b64 s[38:39], -1, 0
	v_mov_b32_e32 v178, v186
	ds_read_b128 v[40:43], v194
	ds_read_b128 v[44:47], v194 offset:1024
	ds_read_b128 v[32:35], v194 offset:2048
	ds_read_b128 v[36:39], v194 offset:3072
	ds_read_b128 v[24:27], v194 offset:4096
	ds_read_b128 v[28:31], v194 offset:5120
	ds_read_b128 v[16:19], v194 offset:6144
	ds_read_b128 v[20:23], v194 offset:7168
	s_add_i32 m0, s31, 0xc000
	s_nop 0
	global_load_lds_dwordx4 v178, s[36:37]
	v_mov_b32_e32 v178, v187
	s_add_i32 m0, s31, 0xe000
	s_nop 0
	global_load_lds_dwordx4 v178, s[36:37]
	s_waitcnt lgkmcnt(8)
	s_barrier
	s_waitcnt lgkmcnt(0)
	s_setprio 1
	s_setprio 0
	s_barrier
	s_and_b64 s[40:41], s[34:35], s[38:39]
	s_andn2_b64 vcc, exec, s[40:41]
	s_cbranch_vccnz .LBB0_5373
	ds_read_b32 v178, v189
	ds_read_b32 v185, v190
	ds_read_b32 v186, v191
	ds_read_b32 v187, v192
	s_waitcnt lgkmcnt(0)
	v_lshl_add_u32 v184, v178, 11, v180
	v_lshl_add_u32 v185, v185, 11, v182
	v_lshl_add_u32 v186, v186, 11, v180
	v_lshl_add_u32 v187, v187, 11, v182
	s_branch .LBB0_5373
.Lpeelg_h1:
	ds_read_b128 v[0:3], v193
	ds_read_b128 v[4:7], v193 offset:1024
	ds_read_b128 v[8:11], v193 offset:2048
	ds_read_b128 v[12:15], v193 offset:3072
	s_cmp_eq_u32 s60, 12
	s_cselect_b64 s[38:39], -1, 0
	v_mov_b32_e32 v178, v186
	ds_read_b128 v[40:43], v194
	ds_read_b128 v[44:47], v194 offset:1024
	ds_read_b128 v[32:35], v194 offset:2048
	ds_read_b128 v[36:39], v194 offset:3072
	ds_read_b128 v[24:27], v194 offset:4096
	ds_read_b128 v[28:31], v194 offset:5120
	ds_read_b128 v[16:19], v194 offset:6144
	ds_read_b128 v[20:23], v194 offset:7168
	s_add_i32 m0, s31, 0xc000
	s_nop 0
	global_load_lds_dwordx4 v178, s[36:37]
	v_mov_b32_e32 v178, v187
	s_add_i32 m0, s31, 0xe000
	s_nop 0
	global_load_lds_dwordx4 v178, s[36:37]
	s_waitcnt lgkmcnt(8)
	s_barrier
	s_waitcnt lgkmcnt(0)
	s_setprio 1
	s_setprio 0
	s_barrier
	s_and_b64 s[40:41], s[34:35], s[38:39]
	s_andn2_b64 vcc, exec, s[40:41]
	s_cbranch_vccnz .Lpeelg_t1
	ds_read_b32 v178, v189
	ds_read_b32 v185, v190
	ds_read_b32 v186, v191
	ds_read_b32 v187, v192
	s_waitcnt lgkmcnt(0)
	v_lshl_add_u32 v184, v178, 11, v180
	v_lshl_add_u32 v185, v185, 11, v182
	v_lshl_add_u32 v186, v186, 11, v180
	v_lshl_add_u32 v187, v187, 11, v182
	s_branch .Lpeelg_t1
